# speedup vs baseline: 1.0326x; 1.0105x over previous
.Lnearslow_ret_A:
	v_pk_mul_f32 v[78:79], v[40:41], v[76:77] op_sel_hi:[0,1]
	v_cmp_eq_u32_e64 s[6:7], 1, v117
	v_cmp_eq_u32_e64 s[26:27], 2, v117
	ds_write_b64 v137, v[78:79]
	ds_read2_b64 v[56:59], v156 offset1:2
	ds_read_b64 v[82:83], v118
	ds_read_b64 v[84:85], v119
	ds_read_b64 v[86:87], v136
	s_waitcnt lgkmcnt(6)
	v_pk_add_f32 v[120:121], v[120:121], v[124:125]
	v_pk_add_f32 v[122:123], v[122:123], v[126:127]
	v_pk_add_f32 v[128:129], v[128:129], v[132:133]
	v_pk_add_f32 v[130:131], v[130:131], v[134:135]
	v_pk_add_f32 v[140:141], v[140:141], v[144:145]
	v_pk_add_f32 v[142:143], v[142:143], v[146:147]
	v_pk_add_f32 v[148:149], v[148:149], v[152:153]
	v_pk_add_f32 v[150:151], v[150:151], v[154:155]
	s_bitcmp1_b32 s21, 8
	s_cbranch_scc1 .Lfarslow_A
.Lfarslow_ret_A:
	v_pk_add_f32 v[120:121], v[120:121], v[128:129]
	v_pk_add_f32 v[122:123], v[122:123], v[130:131]
	v_pk_add_f32 v[140:141], v[140:141], v[148:149]
	v_pk_add_f32 v[142:143], v[142:143], v[150:151]
	v_pk_add_f32 v[120:121], v[120:121], v[140:141]
	v_pk_add_f32 v[122:123], v[122:123], v[142:143]
	v_add_u32_e32 v138, 0xfffffe00, v138
	v_add_u32_e32 v139, 0xffffff00, v139
	v_permlane32_swap_b32_e32 v120, v122
	v_permlane32_swap_b32_e32 v121, v123
	v_pk_add_f32 v[62:63], v[120:121], v[122:123]
	s_bitcmp1_b32 s4, 9
	s_cbranch_scc1 .Lslowlev_A
	s_mov_b64 exec, s[6:7]
	s_waitcnt lgkmcnt(2)
	v_pk_fma_f32 v[80:81], v[40:41], v[82:83], v[78:79] op_sel_hi:[0,1,1]
	s_waitcnt lgkmcnt(1)
	v_pk_fma_f32 v[80:81], v[40:41], v[84:85], v[80:81] op_sel_hi:[0,1,1]
	s_waitcnt lgkmcnt(0)
	v_pk_fma_f32 v[80:81], v[40:41], v[86:87], v[80:81] op_sel_hi:[0,1,1]
	ds_write_b64 v137, v[80:81]
	s_mov_b64 exec, -1
	s_cmp_lt_u32 s9, 2
	s_cbranch_scc1 .Lnp_A
	ds_read_b64 v[82:83], v118
	ds_read_b64 v[84:85], v119
	ds_read_b64 v[86:87], v136
	v_add_u32_sdwa v88, v116, v50 dst_sel:DWORD dst_unused:UNUSED_PAD src0_sel:DWORD src1_sel:WORD_0
	v_add_u32_sdwa v89, v116, v50 dst_sel:DWORD dst_unused:UNUSED_PAD src0_sel:DWORD src1_sel:WORD_1
	v_add_u32_sdwa v90, v116, v51 dst_sel:DWORD dst_unused:UNUSED_PAD src0_sel:DWORD src1_sel:WORD_0
	v_add_u32_sdwa v91, v116, v51 dst_sel:DWORD dst_unused:UNUSED_PAD src0_sel:DWORD src1_sel:WORD_1
	v_bfe_u32 v168, v49, 16, 7
	v_add_u32_sdwa v169, v116, v47 dst_sel:DWORD dst_unused:UNUSED_PAD src0_sel:DWORD src1_sel:WORD_0
	v_add_u32_sdwa v170, v116, v47 dst_sel:DWORD dst_unused:UNUSED_PAD src0_sel:DWORD src1_sel:WORD_1
	v_add_u32_sdwa v171, v116, v49 dst_sel:DWORD dst_unused:UNUSED_PAD src0_sel:DWORD src1_sel:WORD_0
	v_add_u32_e32 v156, 0xfffffa00, v156
	v_add_u32_e32 v172, 0xfffffe00, v137
	v_readlane_b32 s4, v60, s5
	v_max_i32_e32 v156, v156, v162
	v_lshl_add_u64 v[158:159], v[158:159], 0, s[2:3]
	s_and_b32 s23, s21, 0xff
	s_mov_b64 exec, s[26:27]
	s_waitcnt lgkmcnt(2)
	v_pk_fma_f32 v[80:81], v[40:41], v[82:83], v[78:79] op_sel_hi:[0,1,1]
	s_waitcnt lgkmcnt(1)
	v_pk_fma_f32 v[80:81], v[40:41], v[84:85], v[80:81] op_sel_hi:[0,1,1]
	s_waitcnt lgkmcnt(0)
	v_pk_fma_f32 v[80:81], v[40:41], v[86:87], v[80:81] op_sel_hi:[0,1,1]
	ds_write_b64 v137, v[80:81]
	s_mov_b64 exec, -1
	s_cmp_lt_u32 s9, 3
	s_cbranch_scc1 .Lbot_A
	s_mov_b32 s8, 3
.Llev_A:
	ds_read_b64 v[82:83], v118
	ds_read_b64 v[84:85], v119
	ds_read_b64 v[86:87], v136
	v_cmp_eq_u32_e64 s[6:7], s8, v117
	s_add_u32 s8, s8, 1
	s_mov_b64 exec, s[6:7]
	s_waitcnt lgkmcnt(2)
	v_pk_fma_f32 v[80:81], v[40:41], v[82:83], v[78:79] op_sel_hi:[0,1,1]
	s_waitcnt lgkmcnt(1)
	v_pk_fma_f32 v[80:81], v[40:41], v[84:85], v[80:81] op_sel_hi:[0,1,1]
	s_waitcnt lgkmcnt(0)
	v_pk_fma_f32 v[80:81], v[40:41], v[86:87], v[80:81] op_sel_hi:[0,1,1]
	ds_write_b64 v137, v[80:81]
	s_mov_b64 exec, -1
	s_cmp_le_u32 s8, s9
	s_cbranch_scc1 .Llev_A

.Lnearslow_ret_B:
	v_pk_mul_f32 v[78:79], v[48:49], v[76:77] op_sel_hi:[0,1]
	v_cmp_eq_u32_e64 s[6:7], 1, v168
	v_cmp_eq_u32_e64 s[26:27], 2, v168
	ds_write_b64 v172, v[78:79]
	ds_read2_b64 v[52:55], v156 offset1:2
	ds_read_b64 v[82:83], v169
	ds_read_b64 v[84:85], v170
	ds_read_b64 v[86:87], v171
	s_waitcnt lgkmcnt(6)
	v_pk_add_f32 v[120:121], v[120:121], v[124:125]
	v_pk_add_f32 v[122:123], v[122:123], v[126:127]
	v_pk_add_f32 v[128:129], v[128:129], v[132:133]
	v_pk_add_f32 v[130:131], v[130:131], v[134:135]
	v_pk_add_f32 v[140:141], v[140:141], v[144:145]
	v_pk_add_f32 v[142:143], v[142:143], v[146:147]
	v_pk_add_f32 v[148:149], v[148:149], v[152:153]
	v_pk_add_f32 v[150:151], v[150:151], v[154:155]
	s_bitcmp1_b32 s4, 8
	s_cbranch_scc1 .Lfarslow_B
.Lfarslow_ret_B:
	v_pk_add_f32 v[120:121], v[120:121], v[128:129]
	v_pk_add_f32 v[122:123], v[122:123], v[130:131]
	v_pk_add_f32 v[140:141], v[140:141], v[148:149]
	v_pk_add_f32 v[142:143], v[142:143], v[150:151]
	v_pk_add_f32 v[120:121], v[120:121], v[140:141]
	v_pk_add_f32 v[122:123], v[122:123], v[142:143]
	v_add_u32_e32 v138, 0xfffffe00, v138
	v_add_u32_e32 v139, 0xffffff00, v139
	v_permlane32_swap_b32_e32 v120, v122
	v_permlane32_swap_b32_e32 v121, v123
	v_pk_add_f32 v[44:45], v[120:121], v[122:123]
	s_bitcmp1_b32 s21, 9
	s_cbranch_scc1 .Lslowlev_B
	s_mov_b64 exec, s[6:7]
	s_waitcnt lgkmcnt(2)
	v_pk_fma_f32 v[80:81], v[48:49], v[82:83], v[78:79] op_sel_hi:[0,1,1]
	s_waitcnt lgkmcnt(1)
	v_pk_fma_f32 v[80:81], v[48:49], v[84:85], v[80:81] op_sel_hi:[0,1,1]
	s_waitcnt lgkmcnt(0)
	v_pk_fma_f32 v[80:81], v[48:49], v[86:87], v[80:81] op_sel_hi:[0,1,1]
	ds_write_b64 v172, v[80:81]
	s_mov_b64 exec, -1
	s_cmp_lt_u32 s23, 2
	s_cbranch_scc1 .Lnp_B
	ds_read_b64 v[82:83], v169
	ds_read_b64 v[84:85], v170
	ds_read_b64 v[86:87], v171
	v_add_u32_sdwa v88, v116, v42 dst_sel:DWORD dst_unused:UNUSED_PAD src0_sel:DWORD src1_sel:WORD_0
	v_add_u32_sdwa v89, v116, v42 dst_sel:DWORD dst_unused:UNUSED_PAD src0_sel:DWORD src1_sel:WORD_1
	v_add_u32_sdwa v90, v116, v43 dst_sel:DWORD dst_unused:UNUSED_PAD src0_sel:DWORD src1_sel:WORD_0
	v_add_u32_sdwa v91, v116, v43 dst_sel:DWORD dst_unused:UNUSED_PAD src0_sel:DWORD src1_sel:WORD_1
	v_bfe_u32 v117, v41, 16, 7
	v_add_u32_sdwa v118, v116, v39 dst_sel:DWORD dst_unused:UNUSED_PAD src0_sel:DWORD src1_sel:WORD_0
	v_add_u32_sdwa v119, v116, v39 dst_sel:DWORD dst_unused:UNUSED_PAD src0_sel:DWORD src1_sel:WORD_1
	v_add_u32_sdwa v136, v116, v41 dst_sel:DWORD dst_unused:UNUSED_PAD src0_sel:DWORD src1_sel:WORD_0
	v_add_u32_e32 v156, 0xfffffa00, v156
	v_add_u32_e32 v137, 0xfffffe00, v172
	v_readlane_b32 s21, v60, s5
	v_max_i32_e32 v156, v156, v162
	v_lshl_add_u64 v[158:159], v[158:159], 0, s[2:3]
	s_and_b32 s9, s4, 0xff
	s_mov_b64 exec, s[26:27]
	s_waitcnt lgkmcnt(2)
	v_pk_fma_f32 v[80:81], v[48:49], v[82:83], v[78:79] op_sel_hi:[0,1,1]
	s_waitcnt lgkmcnt(1)
	v_pk_fma_f32 v[80:81], v[48:49], v[84:85], v[80:81] op_sel_hi:[0,1,1]
	s_waitcnt lgkmcnt(0)
	v_pk_fma_f32 v[80:81], v[48:49], v[86:87], v[80:81] op_sel_hi:[0,1,1]
	ds_write_b64 v172, v[80:81]
	s_mov_b64 exec, -1
	s_cmp_lt_u32 s23, 3
	s_cbranch_scc1 .Lbot_B
	s_mov_b32 s8, 3
.Llev_B:
	ds_read_b64 v[82:83], v169
	ds_read_b64 v[84:85], v170
	ds_read_b64 v[86:87], v171
	v_cmp_eq_u32_e64 s[6:7], s8, v168
	s_add_u32 s8, s8, 1
	s_mov_b64 exec, s[6:7]
	s_waitcnt lgkmcnt(2)
	v_pk_fma_f32 v[80:81], v[48:49], v[82:83], v[78:79] op_sel_hi:[0,1,1]
	s_waitcnt lgkmcnt(1)
	v_pk_fma_f32 v[80:81], v[48:49], v[84:85], v[80:81] op_sel_hi:[0,1,1]
	s_waitcnt lgkmcnt(0)
	v_pk_fma_f32 v[80:81], v[48:49], v[86:87], v[80:81] op_sel_hi:[0,1,1]
	ds_write_b64 v172, v[80:81]
	s_mov_b64 exec, -1
	s_cmp_le_u32 s8, s23
	s_cbranch_scc1 .Llev_B
